# v69 + fused running-sum update (v_fma into l register, drops one v_mov per softmax block)
# baseline (speedup 1.0000x reference)
.LBB0_1066:
	v_exp_f32_e32 v50, v50
	v_exp_f32_e32 v34, v34
	v_exp_f32_e32 v51, v51
	v_exp_f32_e32 v35, v35
	v_exp_f32_e32 v52, v52
	v_exp_f32_e32 v53, v53
	v_exp_f32_e32 v36, v36
	v_exp_f32_e32 v37, v37
	v_exp_f32_e32 v54, v54
	v_exp_f32_e32 v55, v55
	v_exp_f32_e32 v38, v38
	v_exp_f32_e32 v39, v39
	v_pk_add_f32 v[92:93], v[34:35], v[50:51]
	v_exp_f32_e32 v56, v56
	v_exp_f32_e32 v57, v57
	v_pk_add_f32 v[92:93], v[52:53], v[92:93]
	v_exp_f32_e32 v40, v40
	v_exp_f32_e32 v41, v41
	v_pk_add_f32 v[92:93], v[36:37], v[92:93]
	v_exp_f32_e32 v58, v58
	v_exp_f32_e32 v59, v59
	v_pk_add_f32 v[92:93], v[54:55], v[92:93]
	v_exp_f32_e32 v42, v42
	v_exp_f32_e32 v43, v43
	v_pk_add_f32 v[92:93], v[38:39], v[92:93]
	v_exp_f32_e32 v60, v60
	v_exp_f32_e32 v61, v61
	v_pk_add_f32 v[92:93], v[56:57], v[92:93]
	v_exp_f32_e32 v44, v44
	v_exp_f32_e32 v45, v45
	v_pk_add_f32 v[92:93], v[40:41], v[92:93]
	v_exp_f32_e32 v62, v62
	v_exp_f32_e32 v63, v63
	v_pk_add_f32 v[92:93], v[58:59], v[92:93]
	v_exp_f32_e32 v46, v46
	v_exp_f32_e32 v47, v47
	v_pk_add_f32 v[92:93], v[42:43], v[92:93]
	v_exp_f32_e32 v64, v64
	v_exp_f32_e32 v65, v65
	v_pk_add_f32 v[92:93], v[60:61], v[92:93]
	v_exp_f32_e32 v48, v48
	v_exp_f32_e32 v49, v49
	v_pk_add_f32 v[92:93], v[44:45], v[92:93]
	v_cvt_pk_bf16_f32 v90, v50, v51
	v_pk_add_f32 v[92:93], v[62:63], v[92:93]
	v_cvt_pk_bf16_f32 v94, v58, v59
	v_pk_add_f32 v[92:93], v[46:47], v[92:93]
	v_cvt_pk_bf16_f32 v95, v60, v61
	v_pk_add_f32 v[92:93], v[64:65], v[92:93]
	v_cvt_pk_bf16_f32 v96, v62, v63
	v_pk_add_f32 v[92:93], v[48:49], v[92:93]
	v_cvt_pk_bf16_f32 v97, v64, v65
	v_add_f32_e32 v125, v92, v93
	v_fma_f32 v124, v124, v91, v125
	v_cvt_pk_bf16_f32 v91, v52, v53
	v_cvt_pk_bf16_f32 v92, v54, v55
	v_cvt_pk_bf16_f32 v93, v56, v57
	v_cvt_pk_bf16_f32 v98, v34, v35
	v_cvt_pk_bf16_f32 v99, v36, v37
	v_cvt_pk_bf16_f32 v100, v38, v39
	v_cvt_pk_bf16_f32 v101, v40, v41
	v_cvt_pk_bf16_f32 v102, v42, v43
	v_cvt_pk_bf16_f32 v103, v44, v45
	v_cvt_pk_bf16_f32 v104, v46, v47
	v_cvt_pk_bf16_f32 v105, v48, v49
	v_permlane32_swap_b32_e32 v90, v92
	v_permlane32_swap_b32_e32 v91, v93
	v_permlane32_swap_b32_e32 v94, v96
	v_permlane32_swap_b32_e32 v95, v97
	v_permlane32_swap_b32_e32 v98, v100
	v_permlane32_swap_b32_e32 v99, v101
	v_permlane32_swap_b32_e32 v102, v104
	v_permlane32_swap_b32_e32 v103, v105
	s_and_b64 vcc, exec, s[6:7]
	s_mov_b64 s[12:13], -1
	s_cbranch_vccz .LBB0_1046

.LBB0_1117:
	v_exp_f32_e32 v66, v66
	v_exp_f32_e32 v82, v82
	v_exp_f32_e32 v67, v67
	v_exp_f32_e32 v83, v83
	v_exp_f32_e32 v68, v68
	v_exp_f32_e32 v69, v69
	v_exp_f32_e32 v84, v84
	v_exp_f32_e32 v85, v85
	v_exp_f32_e32 v70, v70
	v_exp_f32_e32 v71, v71
	v_exp_f32_e32 v86, v86
	v_exp_f32_e32 v87, v87
	v_pk_add_f32 v[116:117], v[82:83], v[66:67]
	v_exp_f32_e32 v72, v72
	v_exp_f32_e32 v73, v73
	v_pk_add_f32 v[116:117], v[68:69], v[116:117]
	v_exp_f32_e32 v88, v88
	v_exp_f32_e32 v89, v89
	v_pk_add_f32 v[116:117], v[84:85], v[116:117]
	v_exp_f32_e32 v74, v74
	v_exp_f32_e32 v75, v75
	v_pk_add_f32 v[116:117], v[70:71], v[116:117]
	v_exp_f32_e32 v90, v90
	v_exp_f32_e32 v91, v91
	v_pk_add_f32 v[116:117], v[86:87], v[116:117]
	v_exp_f32_e32 v76, v76
	v_exp_f32_e32 v77, v77
	v_pk_add_f32 v[116:117], v[72:73], v[116:117]
	v_exp_f32_e32 v92, v92
	v_exp_f32_e32 v93, v93
	v_pk_add_f32 v[116:117], v[88:89], v[116:117]
	v_exp_f32_e32 v78, v78
	v_exp_f32_e32 v79, v79
	v_pk_add_f32 v[116:117], v[74:75], v[116:117]
	v_exp_f32_e32 v94, v94
	v_exp_f32_e32 v95, v95
	v_pk_add_f32 v[116:117], v[90:91], v[116:117]
	v_exp_f32_e32 v80, v80
	v_exp_f32_e32 v81, v81
	v_pk_add_f32 v[116:117], v[76:77], v[116:117]
	v_exp_f32_e32 v96, v96
	v_exp_f32_e32 v97, v97
	v_pk_add_f32 v[116:117], v[92:93], v[116:117]
	v_cvt_pk_bf16_f32 v115, v68, v69
	v_pk_add_f32 v[116:117], v[78:79], v[116:117]
	v_cvt_pk_bf16_f32 v118, v74, v75
	v_pk_add_f32 v[116:117], v[94:95], v[116:117]
	v_cvt_pk_bf16_f32 v119, v76, v77
	v_pk_add_f32 v[116:117], v[80:81], v[116:117]
	v_cvt_pk_bf16_f32 v120, v78, v79
	v_pk_add_f32 v[116:117], v[96:97], v[116:117]
	v_cvt_pk_bf16_f32 v121, v80, v81
	v_add_f32_e32 v0, v116, v117
	v_fma_f32 v171, v171, v114, v0
	v_cvt_pk_bf16_f32 v114, v66, v67
	v_cvt_pk_bf16_f32 v116, v70, v71
	v_cvt_pk_bf16_f32 v117, v72, v73
	v_cvt_pk_bf16_f32 v122, v82, v83
	v_cvt_pk_bf16_f32 v123, v84, v85
	v_cvt_pk_bf16_f32 v124, v86, v87
	v_cvt_pk_bf16_f32 v125, v88, v89
	v_cvt_pk_bf16_f32 v126, v90, v91
	v_cvt_pk_bf16_f32 v127, v92, v93
	v_cvt_pk_bf16_f32 v128, v94, v95
	v_cvt_pk_bf16_f32 v129, v96, v97
	v_permlane32_swap_b32_e32 v114, v116
	v_permlane32_swap_b32_e32 v115, v117
	v_permlane32_swap_b32_e32 v118, v120
	v_permlane32_swap_b32_e32 v119, v121
	v_permlane32_swap_b32_e32 v122, v124
	v_permlane32_swap_b32_e32 v123, v125
	v_permlane32_swap_b32_e32 v126, v128
	v_permlane32_swap_b32_e32 v127, v129
	s_and_b64 vcc, exec, s[6:7]
	s_mov_b64 s[12:13], -1
	s_cbranch_vccz .LBB0_1097
